# baseline (speedup 1.0000x reference)
.LBB1_12:
	s_or_b64 exec, exec, s[14:15]
	s_waitcnt lgkmcnt(0)
	s_and_b32 s17, s17, 0xffff
	s_mov_b32 s19, 0x20000
	s_mov_b32 s18, 0x12c0000
	v_lshlrev_b32_e32 v51, 1, v7
	s_cmp_lg_u32 s3, 0
	s_mulk_i32 s11, 0x2580
	s_cbranch_scc0 .LBB1_167
	s_add_i32 s15, s11, 0xffffb500
	s_add_i32 s14, s11, 0xffff8f80
	s_add_i32 s28, s11, 0xffffda80
	buffer_load_ushort v7, v51, s[16:19], s15 offen nt
	buffer_load_ushort v8, v51, s[16:19], s28 offen nt
	buffer_load_ushort v9, v51, s[16:19], s14 offen nt
	s_waitcnt vmcnt(2)
	v_cvt_f32_f16_e32 v14, v7
	s_waitcnt vmcnt(1)
	v_cvt_f32_f16_e32 v13, v8
	s_waitcnt vmcnt(0)
	v_cvt_f32_f16_e32 v12, v9
	s_mul_hi_i32 s14, s10, 0x9c000
	s_mul_i32 s15, s10, 0x9c000
	s_cbranch_execnz .LBB1_15

.LBB1_15:
	s_add_i32 s10, s11, 0x2580
	s_add_i32 s12, s11, 0x4b00
	s_add_i32 s13, s11, 0x7080
	s_add_i32 s28, s11, 0x9600
	s_add_i32 s29, s11, 0xbb80
	s_add_i32 s31, s11, 0xe100
	s_add_i32 s33, s11, 0x10680
	buffer_load_ushort v20, v51, s[16:19], s11 offen nt
	buffer_load_ushort v22, v51, s[16:19], s10 offen nt
	buffer_load_ushort v18, v51, s[16:19], s12 offen nt
	buffer_load_ushort v21, v51, s[16:19], s13 offen nt
	buffer_load_ushort v16, v51, s[16:19], s28 offen nt
	buffer_load_ushort v19, v51, s[16:19], s29 offen nt
	buffer_load_ushort v15, v51, s[16:19], s31 offen nt
	buffer_load_ushort v17, v51, s[16:19], s33 offen nt
	s_add_i32 s10, s11, 0x12c00
	s_add_i32 s12, s11, 0x15180
	s_add_i32 s13, s11, 0x17700
	s_add_i32 s28, s11, 0x19c80
	s_add_i32 s29, s11, 0x1c200
	s_add_i32 s31, s11, 0x1e780
	s_add_i32 s33, s11, 0x20d00
	s_add_i32 s34, s11, 0x23280
	buffer_load_ushort v28, v51, s[16:19], s10 offen nt
	buffer_load_ushort v30, v51, s[16:19], s12 offen nt
	buffer_load_ushort v26, v51, s[16:19], s13 offen nt
	buffer_load_ushort v29, v51, s[16:19], s28 offen nt
	buffer_load_ushort v24, v51, s[16:19], s29 offen nt
	buffer_load_ushort v27, v51, s[16:19], s31 offen nt
	buffer_load_ushort v23, v51, s[16:19], s33 offen nt
	buffer_load_ushort v25, v51, s[16:19], s34 offen nt
	s_add_i32 s10, s11, 0x25800
	s_add_i32 s12, s11, 0x27d80
	s_add_i32 s13, s11, 0x2a300
	s_add_i32 s28, s11, 0x2c880
	s_add_i32 s29, s11, 0x2ee00
	s_add_i32 s31, s11, 0x31380
	s_add_i32 s33, s11, 0x33900
	s_add_i32 s34, s11, 0x35e80
	buffer_load_ushort v36, v51, s[16:19], s10 offen nt
	buffer_load_ushort v38, v51, s[16:19], s12 offen nt
	buffer_load_ushort v34, v51, s[16:19], s13 offen nt
	buffer_load_ushort v37, v51, s[16:19], s28 offen nt
	buffer_load_ushort v32, v51, s[16:19], s29 offen nt
	buffer_load_ushort v35, v51, s[16:19], s31 offen nt
	buffer_load_ushort v31, v51, s[16:19], s33 offen nt
	buffer_load_ushort v33, v51, s[16:19], s34 offen nt
	s_add_i32 s10, s11, 0x38400
	s_add_i32 s12, s11, 0x3a980
	s_add_i32 s13, s11, 0x3cf00
	s_add_i32 s28, s11, 0x3f480
	s_add_i32 s29, s11, 0x41a00
	s_add_i32 s31, s11, 0x43f80
	s_add_i32 s33, s11, 0x46500
	s_add_i32 s34, s11, 0x48a80
	buffer_load_ushort v44, v51, s[16:19], s10 offen nt
	buffer_load_ushort v46, v51, s[16:19], s12 offen nt
	buffer_load_ushort v42, v51, s[16:19], s13 offen nt
	buffer_load_ushort v45, v51, s[16:19], s28 offen nt
	buffer_load_ushort v40, v51, s[16:19], s29 offen nt
	buffer_load_ushort v43, v51, s[16:19], s31 offen nt
	buffer_load_ushort v39, v51, s[16:19], s33 offen nt
	buffer_load_ushort v41, v51, s[16:19], s34 offen nt
	s_add_i32 s10, s11, 0x4b000
	s_add_i32 s12, s11, 0x4d580
	s_add_i32 s13, s11, 0x4fb00
	s_add_i32 s28, s11, 0x52080
	s_add_i32 s29, s11, 0x54600
	s_add_i32 s31, s11, 0x56b80
	s_add_i32 s33, s11, 0x59100
	s_add_i32 s34, s11, 0x5b680
	buffer_load_ushort v48, v51, s[16:19], s10 offen nt
	buffer_load_ushort v49, v51, s[16:19], s12 offen nt
	buffer_load_ushort v70, v51, s[16:19], s13 offen nt
	buffer_load_ushort v72, v51, s[16:19], s28 offen nt
	buffer_load_ushort v68, v51, s[16:19], s29 offen nt
	buffer_load_ushort v71, v51, s[16:19], s31 offen nt
	buffer_load_ushort v47, v51, s[16:19], s33 offen nt
	buffer_load_ushort v69, v51, s[16:19], s34 offen nt
	s_add_i32 s10, s11, 0x5dc00
	s_add_i32 s12, s11, 0x60180
	s_add_i32 s13, s11, 0x62700
	s_add_i32 s28, s11, 0x64c80
	s_add_i32 s29, s11, 0x67200
	s_add_i32 s31, s11, 0x69780
	s_add_i32 s33, s11, 0x6bd00
	s_add_i32 s34, s11, 0x6e280
	buffer_load_ushort v78, v51, s[16:19], s10 offen nt
	buffer_load_ushort v80, v51, s[16:19], s12 offen nt
	buffer_load_ushort v76, v51, s[16:19], s13 offen nt
	buffer_load_ushort v79, v51, s[16:19], s28 offen nt
	buffer_load_ushort v74, v51, s[16:19], s29 offen nt
	buffer_load_ushort v77, v51, s[16:19], s31 offen nt
	buffer_load_ushort v73, v51, s[16:19], s33 offen nt
	buffer_load_ushort v75, v51, s[16:19], s34 offen nt
	s_add_i32 s10, s11, 0x70800
	s_add_i32 s12, s11, 0x72d80
	s_add_i32 s13, s11, 0x75300
	s_add_i32 s28, s11, 0x77880
	s_add_i32 s29, s11, 0x79e00
	s_add_i32 s31, s11, 0x7c380
	s_add_i32 s33, s11, 0x7e900
	s_add_i32 s34, s11, 0x80e80
	buffer_load_ushort v87, v51, s[16:19], s10 offen nt
	buffer_load_ushort v89, v51, s[16:19], s12 offen nt
	buffer_load_ushort v85, v51, s[16:19], s13 offen nt
	buffer_load_ushort v88, v51, s[16:19], s28 offen nt
	buffer_load_ushort v83, v51, s[16:19], s29 offen nt
	buffer_load_ushort v86, v51, s[16:19], s31 offen nt
	buffer_load_ushort v82, v51, s[16:19], s33 offen nt
	buffer_load_ushort v84, v51, s[16:19], s34 offen nt
	s_add_i32 s10, s11, 0x83400
	s_add_i32 s12, s11, 0x85980
	s_add_i32 s13, s11, 0x87f00
	s_add_i32 s28, s11, 0x8a480
	s_add_i32 s29, s11, 0x8ca00
	s_add_i32 s31, s11, 0x8ef80
	s_add_i32 s33, s11, 0x91500
	s_add_i32 s11, s11, 0x93a80
	buffer_load_ushort v90, v51, s[16:19], s10 offen nt
	buffer_load_ushort v92, v51, s[16:19], s12 offen nt
	buffer_load_ushort v81, v51, s[16:19], s13 offen nt
	buffer_load_ushort v91, v51, s[16:19], s28 offen nt
	buffer_load_ushort v9, v51, s[16:19], s29 offen nt
	buffer_load_ushort v7, v51, s[16:19], s31 offen nt
	buffer_load_ushort v8, v51, s[16:19], s33 offen nt
	buffer_load_ushort v11, v51, s[16:19], s11 offen nt
	v_add_u32_e32 v164, 0x24600, v173
	v_add_u32_e32 v119, 0x24800, v173
	v_add_u32_e32 v117, 0x24700, v173
	s_and_saveexec_b64 s[10:11], s[8:9]
	s_cbranch_execz .LBB1_19
	s_lshl_b32 s12, s30, 2
	v_mov_b32_e32 v51, s12
	global_load_dword v51, v51, s[20:21]
	s_mov_b32 s8, 0x41a00000
	s_waitcnt vmcnt(0)
	v_add_f32_e32 v50, v50, v51
	v_cmp_nlt_f32_e32 vcc, s8, v50
	s_and_saveexec_b64 s[8:9], vcc
	s_cbranch_execz .LBB1_18
	v_mul_f32_e32 v51, 0x3fb8aa3b, v50
	s_mov_b32 s13, 0x3fb8aa3b
	v_rndne_f32_e32 v52, v51
	v_sub_f32_e32 v53, v51, v52
	v_fma_f32 v51, v50, s13, -v51
	v_fmamk_f32 v51, v50, 0x32a5705f, v51
	v_add_f32_e32 v51, v53, v51
	v_exp_f32_e32 v51, v51
	v_cvt_i32_f32_e32 v52, v52
	s_mov_b32 s13, 0xc2ce8ed0
	v_cmp_ngt_f32_e32 vcc, s13, v50
	s_mov_b32 s13, 0x42b17218
	v_ldexp_f32 v51, v51, v52
	v_cndmask_b32_e32 v51, 0, v51, vcc
	v_mov_b32_e32 v64, 0x7f800000
	v_cmp_nlt_f32_e32 vcc, s13, v50
	s_mov_b32 s13, 0x3f2aaaab
	s_mov_b32 s16, 0x7f800000
	v_cndmask_b32_e32 v65, v64, v51, vcc
	v_add_f32_e32 v52, 1.0, v65
	v_add_f32_e32 v50, -1.0, v52
	v_sub_f32_e32 v51, v50, v52
	v_add_f32_e32 v51, 1.0, v51
	v_sub_f32_e32 v50, v65, v50
	v_add_f32_e32 v53, v50, v51
	v_frexp_mant_f32_e32 v54, v52
	v_cvt_f64_f32_e32 v[50:51], v52
	v_frexp_exp_i32_f64_e32 v50, v[50:51]
	v_cmp_gt_f32_e32 vcc, s13, v54
	s_mov_b32 s13, 0x3f317218
	s_nop 0
	v_subbrev_co_u32_e32 v58, vcc, 0, v50, vcc
	v_sub_u32_e32 v50, 0, v58
	v_ldexp_f32 v51, v52, v50
	v_add_f32_e32 v52, -1.0, v51
	v_add_f32_e32 v54, 1.0, v51
	v_ldexp_f32 v50, v53, v50
	v_add_f32_e32 v53, 1.0, v52
	v_add_f32_e32 v55, -1.0, v54
	v_sub_f32_e32 v53, v51, v53
	v_sub_f32_e32 v51, v51, v55
	v_add_f32_e32 v53, v50, v53
	v_add_f32_e32 v50, v50, v51
	v_add_f32_e32 v59, v54, v50
	v_rcp_f32_e32 v61, v59
	v_sub_f32_e32 v51, v54, v59
	v_add_f32_e32 v60, v50, v51
	v_add_f32_e32 v51, v52, v53
	v_mul_f32_e32 v63, v51, v61
	v_sub_f32_e32 v50, v52, v51
	v_mul_f32_e32 v52, v59, v63
	v_fma_f32 v54, v63, v59, -v52
	v_fmac_f32_e32 v54, v63, v60
	v_add_f32_e32 v62, v53, v50
	v_add_f32_e32 v50, v52, v54
	v_sub_f32_e32 v53, v51, v50
	v_pk_add_f32 v[56:57], v[50:51], v[52:53] neg_lo:[0,1] neg_hi:[0,1]
	v_mov_b32_e32 v55, v50
	v_pk_add_f32 v[50:51], v[56:57], v[54:55] neg_lo:[0,1] neg_hi:[0,1]
	v_cmp_neq_f32_e32 vcc, s16, v65
	v_add_f32_e32 v51, v62, v51
	v_add_f32_e32 v50, v50, v51
	v_add_f32_e32 v51, v53, v50
	v_mul_f32_e32 v62, v61, v51
	v_mul_f32_e32 v52, v59, v62
	v_fma_f32 v54, v62, v59, -v52
	v_fmac_f32_e32 v54, v62, v60
	v_sub_f32_e32 v53, v53, v51
	v_add_f32_e32 v59, v50, v53
	v_add_f32_e32 v50, v52, v54
	v_sub_f32_e32 v53, v51, v50
	v_pk_add_f32 v[56:57], v[50:51], v[52:53] neg_lo:[0,1] neg_hi:[0,1]
	v_mov_b32_e32 v55, v50
	v_pk_add_f32 v[50:51], v[56:57], v[54:55] neg_lo:[0,1] neg_hi:[0,1]
	v_cvt_f32_i32_e32 v52, v58
	v_add_f32_e32 v51, v59, v51
	v_add_f32_e32 v50, v50, v51
	v_add_f32_e32 v50, v53, v50
	v_add_f32_e32 v53, v63, v62
	v_sub_f32_e32 v51, v53, v63
	v_mul_f32_e32 v50, v61, v50
	v_sub_f32_e32 v51, v62, v51
	v_add_f32_e32 v50, v51, v50
	v_add_f32_e32 v54, v53, v50
	v_mul_f32_e32 v56, v54, v54
	v_mov_b32_e32 v51, 0x3ecc95a3
	v_sub_f32_e32 v53, v54, v53
	v_fmac_f32_e32 v51, 0x3e9b6dac, v56
	v_sub_f32_e32 v50, v50, v53
	v_fmaak_f32 v51, v56, v51, 0x3f2aaada
	v_ldexp_f32 v57, v50, 1
	v_mul_f32_e32 v53, v54, v56
	v_mov_b32_e32 v50, 0x3f317218
	v_pk_mul_f32 v[50:51], v[52:53], v[50:51]
	v_ldexp_f32 v55, v54, 1
	v_fma_f32 v53, v52, s13, -v50
	v_fmamk_f32 v54, v52, 0xb102e308, v53
	v_pk_add_f32 v[52:53], v[50:51], v[54:55]
	v_mov_b32_e32 v56, v50
	v_sub_f32_e32 v55, v53, v55
	v_sub_f32_e32 v55, v51, v55
	v_add_f32_e32 v57, v57, v55
	v_pk_add_f32 v[50:51], v[52:53], v[50:51] neg_lo:[0,1] neg_hi:[0,1]
	v_pk_add_f32 v[58:59], v[52:53], v[56:57]
	v_mov_b32_e32 v55, v52
	v_mov_b32_e32 v51, v59
	v_pk_add_f32 v[60:61], v[54:55], v[50:51] neg_lo:[0,1] neg_hi:[0,1]
	v_pk_add_f32 v[50:51], v[54:55], v[50:51]
	v_mov_b32_e32 v56, v57
	v_pk_add_f32 v[54:55], v[50:51], v[52:53] op_sel:[1,0] op_sel_hi:[0,1] neg_lo:[0,1] neg_hi:[0,1]
	v_pk_add_f32 v[62:63], v[58:59], v[54:55] op_sel_hi:[1,0] neg_lo:[0,1] neg_hi:[0,1]
	v_mov_b32_e32 v58, v59
	v_mov_b32_e32 v59, v51
	v_pk_mov_b32 v[54:55], v[52:53], v[54:55] op_sel:[1,0]
	v_mov_b32_e32 v57, v52
	v_pk_add_f32 v[54:55], v[58:59], v[54:55] neg_lo:[0,1] neg_hi:[0,1]
	v_mov_b32_e32 v62, v60
	v_pk_add_f32 v[52:53], v[56:57], v[54:55] neg_lo:[0,1] neg_hi:[0,1]
	v_mov_b32_e32 v61, v51
	v_pk_add_f32 v[54:55], v[62:63], v[52:53]
	s_mov_b32 s13, 0x33800000
	v_pk_add_f32 v[56:57], v[54:55], v[54:55] op_sel:[0,1] op_sel_hi:[1,0]
	s_nop 0
	v_pk_add_f32 v[50:51], v[50:51], v[56:57] op_sel:[1,0] op_sel_hi:[0,1]
	v_mov_b32_e32 v55, v50
	v_pk_add_f32 v[58:59], v[54:55], v[60:61] neg_lo:[0,1] neg_hi:[0,1]
	v_mov_b32_e32 v53, v56
	v_sub_f32_e32 v51, v54, v58
	v_pk_add_f32 v[52:53], v[52:53], v[58:59] neg_lo:[0,1] neg_hi:[0,1]
	v_sub_f32_e32 v51, v60, v51
	v_add_f32_e32 v51, v52, v51
	v_add_f32_e32 v51, v51, v53
	v_add_f32_e32 v50, v50, v51
	v_cndmask_b32_e32 v50, v64, v50, vcc
	v_cmp_lt_f32_e64 vcc, |v65|, s13
	s_nop 1
	v_cndmask_b32_e32 v50, v50, v65, vcc

.LBB3_3:
	s_load_dwordx8 s[4:11], s[0:1], 0x0
	v_bfe_u32 v14, v0, 6, 1
	v_and_b32_e32 v4, 31, v0
	v_lshlrev_b32_e32 v16, 9, v14
	v_mov_b32_e32 v17, 0
	s_bfe_u32 s12, s2, 0x1c0002
	s_waitcnt lgkmcnt(0)
	v_lshl_add_u64 v[2:3], s[4:5], 0, v[16:17]
	v_lshlrev_b32_e32 v16, 4, v4
	s_lshl_b32 s3, s2, 2
	s_mul_i32 s12, s12, 6
	v_lshl_add_u64 v[10:11], v[2:3], 0, v[16:17]
	v_bfe_u32 v2, v0, 5, 1
	v_or_b32_e32 v15, s3, v1
	s_bfe_u32 s3, s2, 0x10001
	v_or_b32_e32 v2, s12, v2
	v_bfe_u32 v18, v15, 1, 2
	s_lshl_b32 s13, s3, 2
	v_lshlrev_b32_e32 v2, 3, v2
	v_or3_b32 v16, s13, v2, v18
	v_lshlrev_b64 v[2:3], 10, v[16:17]
	v_lshl_add_u64 v[2:3], v[10:11], 0, v[2:3]
	global_load_dwordx4 v[6:9], v[2:3], off nt
	v_or_b32_e32 v2, 64, v26
	v_lshrrev_b32_e32 v2, 5, v2
	v_add_lshl_u32 v2, v2, s12, 3
	v_or3_b32 v16, s13, v2, v18
	v_or_b32_e32 v2, 0x80, v26
	v_lshrrev_b32_e32 v2, 5, v2
	v_add_lshl_u32 v2, v2, s12, 3
	v_lshlrev_b64 v[12:13], 10, v[16:17]
	v_or3_b32 v16, s13, v2, v18
	v_lshlrev_b64 v[2:3], 10, v[16:17]
	v_lshl_add_u64 v[2:3], v[10:11], 0, v[2:3]
	global_load_dwordx4 v[2:5], v[2:3], off nt
	v_lshl_add_u64 v[10:11], v[10:11], 0, v[12:13]
	global_load_dwordx4 v[10:13], v[10:11], off nt
	v_lshrrev_b32_e32 v15, 1, v15
	s_lshl_b32 s4, s2, 4
	s_and_b32 s4, s4, 0x1c0
	v_and_b32_e32 v15, 0xe00, v15
	v_or_b32_e32 v15, s4, v15
	v_lshlrev_b32_e32 v16, 3, v18
	v_lshlrev_b32_e32 v14, 2, v14
	v_lshl_or_b32 v15, s3, 5, v15
	s_bfe_u32 s3, s2, 0x30005
	v_or3_b32 v27, v15, v16, v14
	v_mov_b32_e32 v14, 0xc0
	v_mul_u32_u24_e32 v14, s3, v14
	s_movk_i32 s12, 0x2580
	v_mov_b64_e32 v[24:25], s[6:7]
	v_lshlrev_b32_e32 v16, 1, v14
	v_mad_u64_u32 v[14:15], s[4:5], v27, s12, v[24:25]
	v_lshl_add_u64 v[18:19], v[14:15], 0, v[16:17]
	v_lshlrev_b32_e32 v14, 1, v26
	v_mov_b32_e32 v15, v17
	v_lshl_add_u64 v[22:23], v[18:19], 0, v[14:15]
	s_movk_i32 s3, 0x1000
	v_add_co_u32_e32 v18, vcc, s3, v22
	s_mov_b64 s[4:5], 0x1800
	s_nop 0
	v_addc_co_u32_e32 v19, vcc, 0, v23, vcc
	global_load_ushort v36, v[18:19], off offset:2048 nt
	v_mbcnt_lo_u32_b32 v18, -1, 0
	v_mbcnt_hi_u32_b32 v37, -1, v18
	v_and_b32_e32 v18, 64, v37
	v_xor_b32_e32 v19, 1, v37
	v_add_u32_e32 v39, 64, v18
	v_xor_b32_e32 v20, 2, v37
	v_cmp_lt_i32_e32 vcc, v19, v39
	v_xor_b32_e32 v21, 4, v37
	v_xor_b32_e32 v38, 8, v37
	v_cndmask_b32_e32 v18, v37, v19, vcc
	v_cmp_lt_i32_e32 vcc, v20, v39
	v_lshlrev_b32_e32 v40, 2, v18
	v_lshl_add_u64 v[22:23], v[22:23], 0, s[4:5]
	v_cndmask_b32_e32 v19, v37, v20, vcc
	v_cmp_lt_i32_e32 vcc, v21, v39
	v_lshlrev_b32_e32 v41, 2, v19
	global_load_ushort v44, v[22:23], off offset:128 nt
	global_load_ushort v45, v[22:23], off offset:256 nt
	v_cndmask_b32_e32 v20, v37, v21, vcc
	v_lshlrev_b32_e32 v42, 2, v20
	v_cmp_lt_i32_e32 vcc, v38, v39
	v_xor_b32_e32 v43, 16, v37
	v_or_b32_e32 v51, 1, v27
	v_or_b32_e32 v55, 2, v27
	v_or_b32_e32 v56, 3, v27
	s_waitcnt vmcnt(5)
	v_mov_b32_e32 v18, v6
	v_mov_b32_e32 v20, v7
	v_mov_b32_e32 v28, v8
	v_mov_b32_e32 v30, v9
	s_waitcnt vmcnt(4)
	v_mov_b32_e32 v19, v2
	v_mov_b32_e32 v21, v3
	v_mov_b32_e32 v29, v4
	v_pk_mul_f32 v[32:33], v[18:19], v[18:19]
	v_pk_mul_f32 v[34:35], v[20:21], v[20:21]
	v_pk_mul_f32 v[18:19], v[28:29], v[28:29]
	v_cndmask_b32_e32 v28, v37, v38, vcc
	v_lshlrev_b32_e32 v38, 2, v28
	v_mov_b32_e32 v28, v32
	v_mov_b32_e32 v29, v34
	s_waitcnt vmcnt(3)
	v_pk_fma_f32 v[28:29], v[10:11], v[10:11], v[28:29]
	v_mov_b32_e32 v34, v33
	v_mov_b32_e32 v31, v5
	v_pk_add_f32 v[28:29], v[28:29], v[34:35]
	v_pk_mul_f32 v[20:21], v[30:31], v[30:31]
	ds_bpermute_b32 v30, v40, v28
	ds_bpermute_b32 v31, v40, v29
	v_cmp_lt_i32_e32 vcc, v43, v39
	s_waitcnt lgkmcnt(0)
	v_pk_add_f32 v[22:23], v[28:29], v[30:31]
	ds_bpermute_b32 v28, v41, v22
	ds_bpermute_b32 v29, v41, v23
	v_cndmask_b32_e32 v30, v37, v43, vcc
	v_lshlrev_b32_e32 v43, 2, v26
	global_load_dword v46, v43, s[8:9]
	global_load_dword v49, v43, s[8:9] offset:256
	global_load_dword v50, v43, s[8:9] offset:512
	s_waitcnt lgkmcnt(0)
	v_pk_add_f32 v[22:23], v[22:23], v[28:29]
	ds_bpermute_b32 v28, v42, v22
	ds_bpermute_b32 v29, v42, v23
	v_lshlrev_b32_e32 v47, 2, v30
	v_xor_b32_e32 v30, 32, v37
	v_cmp_lt_i32_e32 vcc, v30, v39
	s_waitcnt vmcnt(5)
	v_cvt_f32_f16_e32 v48, v36
	s_waitcnt lgkmcnt(0)
	v_pk_add_f32 v[22:23], v[22:23], v[28:29]
	ds_bpermute_b32 v28, v38, v22
	ds_bpermute_b32 v29, v38, v23
	v_cndmask_b32_e32 v30, v37, v30, vcc
	v_mul_f32_e32 v34, 0xbfb8aa3b, v48
	v_exp_f32_e32 v53, v34
	v_lshlrev_b32_e32 v39, 2, v30
	s_waitcnt lgkmcnt(0)
	v_pk_add_f32 v[28:29], v[22:23], v[28:29]
	v_mad_u64_u32 v[22:23], s[6:7], v51, s12, v[24:25]
	v_lshl_add_u64 v[22:23], v[22:23], 0, v[16:17]
	v_lshl_add_u64 v[32:33], v[22:23], 0, v[14:15]
	v_add_co_u32_e32 v22, vcc, s3, v32
	ds_bpermute_b32 v30, v47, v28
	s_nop 0
	v_addc_co_u32_e32 v23, vcc, 0, v33, vcc
	global_load_ushort v52, v[22:23], off offset:2048 nt
	v_lshl_add_u64 v[32:33], v[32:33], 0, s[4:5]
	global_load_ushort v54, v[32:33], off offset:128 nt
	v_lshl_add_u64 v[22:23], s[10:11], 0, v[16:17]
	v_mad_u64_u32 v[34:35], s[10:11], v55, s12, v[24:25]
	v_lshl_add_u64 v[34:35], v[34:35], 0, v[16:17]
	v_lshl_add_u64 v[34:35], v[34:35], 0, v[14:15]
	v_mad_u64_u32 v[24:25], s[10:11], v56, s12, v[24:25]
	ds_bpermute_b32 v31, v47, v29
	v_lshl_add_u64 v[36:37], v[34:35], 0, s[4:5]
	v_add_co_u32_e32 v34, vcc, s3, v34
	v_lshl_add_u64 v[16:17], v[24:25], 0, v[16:17]
	s_nop 0
	v_addc_co_u32_e32 v35, vcc, 0, v35, vcc
	v_lshl_add_u64 v[16:17], v[16:17], 0, v[14:15]
	v_lshl_add_u64 v[24:25], v[16:17], 0, s[4:5]
	global_load_ushort v57, v[34:35], off offset:2048 nt
	global_load_ushort v58, v[36:37], off offset:128 nt
	global_load_ushort v59, v[24:25], off offset:128 nt
	global_load_ushort v60, v[24:25], off offset:256 nt
	global_load_ushort v61, v[36:37], off offset:256 nt
	global_load_ushort v62, v[32:33], off offset:256 nt
	s_waitcnt lgkmcnt(0)
	v_pk_add_f32 v[28:29], v[28:29], v[30:31]
	ds_bpermute_b32 v30, v39, v28
	ds_bpermute_b32 v31, v39, v29
	s_movk_i32 s6, 0xc00
	v_mad_u64_u32 v[24:25], s[4:5], v27, s6, v[22:23]
	s_mov_b32 s10, 0x3727c5ac
	s_waitcnt lgkmcnt(0)
	v_pk_add_f32 v[28:29], v[28:29], v[30:31]
	s_mov_b32 s4, 0x3baaaaab
	v_mov_b64_e32 v[30:31], s[10:11]
	v_pk_fma_f32 v[28:29], v[28:29], s[4:5], v[30:31] op_sel_hi:[1,0,0]
	s_mov_b32 s5, 0x800000
	v_mul_f32_e32 v32, 0x4b800000, v28
	v_cmp_gt_f32_e32 vcc, s5, v28
	v_add_f32_e32 v27, 1.0, v53
	v_rcp_f32_e32 v27, v27
	v_cndmask_b32_e32 v28, v28, v32, vcc
	s_waitcnt vmcnt(12)
	v_cvt_f32_f16_e32 v32, v44
	v_rsq_f32_e32 v28, v28
	s_waitcnt vmcnt(11)
	v_cvt_f32_f16_e32 v33, v45
	v_lshl_add_u64 v[24:25], v[24:25], 0, v[14:15]
	v_mul_f32_e32 v37, 0xbfb8aa3b, v32
	v_mul_f32_e32 v34, 0x45800000, v28
	v_exp_f32_e32 v37, v37
	v_cndmask_b32_e32 v28, v28, v34, vcc
	v_mul_f32_e32 v6, v28, v6
	global_load_dword v34, v43, s[8:9] offset:512
	global_load_dword v35, v43, s[8:9] offset:256
	global_load_dword v36, v43, s[8:9]
	v_add_f32_e32 v37, 1.0, v37
	v_rcp_f32_e32 v37, v37
	v_cmp_gt_f32_e32 vcc, s5, v29
	v_mul_f32_e32 v2, v28, v2
	s_waitcnt vmcnt(13)
	v_mul_f32_e32 v6, v6, v46
	v_mul_f32_e32 v6, v6, v48
	v_fma_mixlo_f16 v6, v6, v27, 0
	v_mul_f32_e32 v27, 0xbfb8aa3b, v33
	v_exp_f32_e32 v27, v27
	global_store_short v[24:25], v6, off
	v_mul_f32_e32 v6, v28, v10
	s_waitcnt vmcnt(13)
	v_mul_f32_e32 v6, v6, v49
	v_mul_f32_e32 v6, v6, v32
	v_fma_mixlo_f16 v6, v6, v37, 0
	v_add_f32_e32 v27, 1.0, v27
	global_store_short v[24:25], v6, off offset:128
	v_mul_f32_e32 v6, 0x4b800000, v29
	v_rcp_f32_e32 v27, v27
	v_cndmask_b32_e32 v6, v29, v6, vcc
	v_rsq_f32_e32 v6, v6
	s_waitcnt vmcnt(13)
	v_mul_f32_e32 v2, v2, v50
	v_mul_f32_e32 v2, v2, v33
	v_fma_mixlo_f16 v2, v2, v27, 0
	global_store_short v[24:25], v2, off offset:256
	v_mul_f32_e32 v2, 0x45800000, v6
	v_cndmask_b32_e32 v2, v6, v2, vcc
	v_mul_f32_e32 v7, v2, v7
	v_mul_f32_e32 v7, v7, v46
	v_mad_u64_u32 v[24:25], s[8:9], v51, s6, v[22:23]
	s_waitcnt vmcnt(13)
	v_cvt_f32_f16_e32 v10, v52
	s_waitcnt vmcnt(12)
	v_cvt_f32_f16_e32 v27, v54
	v_mul_f32_e32 v6, 0xbfb8aa3b, v10
	v_exp_f32_e32 v6, v6
	v_mul_f32_e32 v7, v7, v10
	v_add_f32_e32 v6, 1.0, v6
	v_rcp_f32_e32 v6, v6
	s_nop 0
	v_fma_mixlo_f16 v10, v7, v6, 0
	v_lshl_add_u64 v[6:7], v[24:25], 0, v[14:15]
	v_mul_f32_e32 v24, 0xbfb8aa3b, v27
	v_exp_f32_e32 v24, v24
	global_store_short v[6:7], v10, off
	v_mul_f32_e32 v10, v2, v11
	v_mul_f32_e32 v25, v10, v49
	v_add_f32_e32 v10, 1.0, v24
	v_rcp_f32_e32 v24, v10
	v_add_co_u32_e32 v10, vcc, s3, v16
	v_mul_f32_e32 v2, v2, v3
	s_nop 0
	v_addc_co_u32_e32 v11, vcc, 0, v17, vcc
	global_load_ushort v28, v[10:11], off offset:2048 nt
	v_mul_f32_e32 v10, v25, v27
	v_fma_mixlo_f16 v10, v10, v24, 0
	global_store_short v[6:7], v10, off offset:128
	v_mov_b32_e32 v10, v18
	v_mov_b32_e32 v11, v20
	v_pk_fma_f32 v[10:11], v[12:13], v[12:13], v[10:11]
	v_mov_b32_e32 v20, v19
	v_pk_add_f32 v[10:11], v[10:11], v[20:21]
	s_waitcnt vmcnt(9)
	v_cvt_f32_f16_e32 v24, v62
	ds_bpermute_b32 v16, v40, v10
	ds_bpermute_b32 v17, v40, v11
	v_mul_f32_e32 v18, v2, v50
	v_mul_f32_e32 v2, 0xbfb8aa3b, v24
	v_exp_f32_e32 v19, v2
	v_cvt_f32_f16_e32 v20, v61
	s_waitcnt lgkmcnt(0)
	v_pk_add_f32 v[2:3], v[10:11], v[16:17]
	ds_bpermute_b32 v10, v41, v2
	ds_bpermute_b32 v11, v41, v3
	v_add_f32_e32 v17, 1.0, v19
	v_rcp_f32_e32 v17, v17
	v_mul_f32_e32 v16, v18, v24
	v_cvt_f32_f16_e32 v18, v57
	s_waitcnt lgkmcnt(0)
	v_pk_add_f32 v[2:3], v[2:3], v[10:11]
	ds_bpermute_b32 v10, v42, v2
	ds_bpermute_b32 v11, v42, v3
	v_fma_mixlo_f16 v16, v16, v17, 0
	global_store_short v[6:7], v16, off offset:256
	v_mul_f32_e32 v6, 0xbfb8aa3b, v18
	v_exp_f32_e32 v16, v6
	s_waitcnt lgkmcnt(0)
	v_pk_add_f32 v[2:3], v[2:3], v[10:11]
	ds_bpermute_b32 v6, v38, v2
	ds_bpermute_b32 v7, v38, v3
	v_cvt_f32_f16_e32 v17, v58
	v_add_f32_e32 v16, 1.0, v16
	v_rcp_f32_e32 v16, v16
	v_mul_f32_e32 v21, 0xbfb8aa3b, v20
	s_waitcnt lgkmcnt(0)
	v_pk_add_f32 v[2:3], v[2:3], v[6:7]
	ds_bpermute_b32 v6, v47, v2
	ds_bpermute_b32 v7, v47, v3
	v_mul_f32_e32 v19, 0xbfb8aa3b, v17
	v_exp_f32_e32 v19, v19
	v_exp_f32_e32 v21, v21
	v_mad_u64_u32 v[10:11], s[8:9], v55, s6, v[22:23]
	s_waitcnt lgkmcnt(0)
	v_pk_add_f32 v[2:3], v[2:3], v[6:7]
	ds_bpermute_b32 v6, v39, v2
	ds_bpermute_b32 v7, v39, v3
	v_add_f32_e32 v19, 1.0, v19
	v_lshl_add_u64 v[10:11], v[10:11], 0, v[14:15]
	s_waitcnt lgkmcnt(0)
	v_pk_add_f32 v[2:3], v[2:3], v[6:7]
	s_nop 0
	v_pk_fma_f32 v[2:3], v[2:3], s[4:5], v[30:31] op_sel_hi:[1,0,0]
	v_add_f32_e32 v7, 1.0, v21
	v_mul_f32_e32 v6, 0x4b800000, v2
	v_cmp_gt_f32_e32 vcc, s5, v2
	v_rcp_f32_e32 v7, v7
	s_nop 0
	v_cndmask_b32_e32 v2, v2, v6, vcc
	v_rsq_f32_e32 v2, v2
	v_rcp_f32_e32 v6, v19
	v_mul_f32_e32 v19, 0x45800000, v2
	v_cndmask_b32_e32 v2, v2, v19, vcc
	v_mul_f32_e32 v8, v2, v8
	s_waitcnt vmcnt(7)
	v_mul_f32_e32 v8, v8, v36
	v_mul_f32_e32 v8, v8, v18
	v_fma_mixlo_f16 v8, v8, v16, 0
	global_store_short v[10:11], v8, off
	v_mul_f32_e32 v8, v2, v12
	v_mul_f32_e32 v2, v2, v4
	v_mul_f32_e32 v4, 0x4b800000, v3
	v_cmp_gt_f32_e32 vcc, s5, v3
	v_mul_f32_e32 v2, v2, v34
	v_mul_f32_e32 v8, v8, v35
	v_cndmask_b32_e32 v3, v3, v4, vcc
	v_rsq_f32_e32 v3, v3
	v_mul_f32_e32 v2, v2, v20
	s_waitcnt vmcnt(3)
	v_cvt_f32_f16_e32 v4, v28
	v_mul_f32_e32 v8, v8, v17
	v_fma_mixlo_f16 v2, v2, v7, 0
	v_fma_mixlo_f16 v6, v8, v6, 0
	global_store_short v[10:11], v2, off offset:256
	v_mul_f32_e32 v2, 0x45800000, v3
	global_store_short v[10:11], v6, off offset:128
	v_cndmask_b32_e32 v6, v3, v2, vcc
	v_mul_f32_e32 v2, 0xbfb8aa3b, v4
	v_exp_f32_e32 v7, v2
	v_mul_f32_e32 v8, v6, v9
	v_mul_f32_e32 v8, v8, v36
	v_mul_f32_e32 v4, v8, v4
	v_add_f32_e32 v7, 1.0, v7
	v_rcp_f32_e32 v7, v7
	v_cvt_f32_f16_e32 v8, v59
	v_mad_u64_u32 v[2:3], s[4:5], v56, s6, v[22:23]
	v_fma_mixlo_f16 v4, v4, v7, 0
	v_lshl_add_u64 v[2:3], v[2:3], 0, v[14:15]
	global_store_short v[2:3], v4, off
	v_mul_f32_e32 v4, 0xbfb8aa3b, v8
	v_exp_f32_e32 v4, v4
	v_cvt_f32_f16_e32 v9, v60
	v_mul_f32_e32 v7, v6, v13
	v_mul_f32_e32 v7, v7, v35
	v_add_f32_e32 v4, 1.0, v4
	v_rcp_f32_e32 v4, v4
	v_mul_f32_e32 v10, 0xbfb8aa3b, v9
	v_exp_f32_e32 v10, v10
	v_mul_f32_e32 v7, v7, v8
	v_fma_mixlo_f16 v4, v7, v4, 0
	global_store_short v[2:3], v4, off offset:128
	v_add_f32_e32 v4, 1.0, v10
	v_rcp_f32_e32 v4, v4
	v_mul_f32_e32 v5, v6, v5
	v_mul_f32_e32 v5, v5, v34
	v_mul_f32_e32 v5, v5, v9
	v_fma_mixlo_f16 v4, v5, v4, 0
	global_store_short v[2:3], v4, off offset:256
	s_cbranch_execnz .LBB3_2
.LBB3_4:
	s_load_dwordx4 s[4:7], s[0:1], 0x20
	s_add_i32 s0, s2, 0xfffffc00
	s_ashr_i32 s1, s0, 31
	s_lshr_b32 s1, s1, 28
	s_add_i32 s1, s0, s1
	s_and_b32 s2, s1, 0x3fffff0
	s_sub_i32 s0, s0, s2
	s_lshl_b32 s0, s0, 6
	s_lshl_b32 s1, s1, 2
	s_and_b32 s2, s1, 0xffffffc0
	s_ashr_i32 s1, s0, 31
	s_lshl_b64 s[8:9], s[0:1], 2
	s_waitcnt lgkmcnt(0)
	s_add_u32 s4, s4, s8
	v_or_b32_e32 v6, s2, v1
	s_addc_u32 s5, s5, s9
	v_lshlrev_b32_e32 v2, 2, v26
	v_mov_b32_e32 v3, 0
	v_ashrrev_i32_e32 v7, 31, v6
	v_or_b32_e32 v10, 4, v6
	v_or_b32_e32 v12, 8, v6
	v_or_b32_e32 v14, 12, v6
	v_or_b32_e32 v16, 16, v6
	v_or_b32_e32 v18, 20, v6
	v_or_b32_e32 v20, 24, v6
	v_or_b32_e32 v22, 28, v6
	v_lshl_add_u64 v[4:5], s[4:5], 0, v[2:3]
	v_lshlrev_b64 v[8:9], 12, v[6:7]
	v_ashrrev_i32_e32 v11, 31, v10
	v_ashrrev_i32_e32 v13, 31, v12
	v_ashrrev_i32_e32 v15, 31, v14
	v_ashrrev_i32_e32 v17, 31, v16
	v_ashrrev_i32_e32 v19, 31, v18
	v_ashrrev_i32_e32 v21, 31, v20
	v_ashrrev_i32_e32 v23, 31, v22
	v_lshl_add_u64 v[8:9], v[4:5], 0, v[8:9]
	v_lshlrev_b64 v[10:11], 12, v[10:11]
	v_lshlrev_b64 v[12:13], 12, v[12:13]
	v_lshlrev_b64 v[14:15], 12, v[14:15]
	v_lshlrev_b64 v[16:17], 12, v[16:17]
	v_lshlrev_b64 v[18:19], 12, v[18:19]
	v_lshlrev_b64 v[20:21], 12, v[20:21]
	v_lshlrev_b64 v[22:23], 12, v[22:23]
	v_lshl_add_u64 v[10:11], v[4:5], 0, v[10:11]
	v_lshl_add_u64 v[12:13], v[4:5], 0, v[12:13]
	v_lshl_add_u64 v[14:15], v[4:5], 0, v[14:15]
	v_lshl_add_u64 v[16:17], v[4:5], 0, v[16:17]
	v_lshl_add_u64 v[18:19], v[4:5], 0, v[18:19]
	v_lshl_add_u64 v[20:21], v[4:5], 0, v[20:21]
	v_lshl_add_u64 v[22:23], v[4:5], 0, v[22:23]
	global_load_dword v24, v[8:9], off nt
	global_load_dword v25, v[10:11], off nt
	global_load_dword v26, v[12:13], off nt
	global_load_dword v27, v[14:15], off nt
	global_load_dword v28, v[16:17], off nt
	global_load_dword v29, v[18:19], off nt
	global_load_dword v30, v[20:21], off nt
	global_load_dword v31, v[22:23], off nt
	v_or_b32_e32 v8, 32, v6
	v_ashrrev_i32_e32 v9, 31, v8
	v_or_b32_e32 v10, 36, v6
	v_or_b32_e32 v12, 40, v6
	v_or_b32_e32 v14, 44, v6
	v_or_b32_e32 v16, 48, v6
	v_or_b32_e32 v18, 52, v6
	v_or_b32_e32 v20, 56, v6
	v_or_b32_e32 v6, 60, v6
	v_lshlrev_b64 v[8:9], 12, v[8:9]
	v_ashrrev_i32_e32 v11, 31, v10
	v_ashrrev_i32_e32 v13, 31, v12
	v_ashrrev_i32_e32 v15, 31, v14
	v_ashrrev_i32_e32 v17, 31, v16
	v_ashrrev_i32_e32 v19, 31, v18
	v_ashrrev_i32_e32 v21, 31, v20
	v_ashrrev_i32_e32 v7, 31, v6
	v_lshl_add_u64 v[8:9], v[4:5], 0, v[8:9]
	v_lshlrev_b64 v[10:11], 12, v[10:11]
	v_lshlrev_b64 v[12:13], 12, v[12:13]
	v_lshlrev_b64 v[14:15], 12, v[14:15]
	v_lshlrev_b64 v[16:17], 12, v[16:17]
	v_lshlrev_b64 v[18:19], 12, v[18:19]
	v_lshlrev_b64 v[20:21], 12, v[20:21]
	v_lshlrev_b64 v[6:7], 12, v[6:7]
	v_lshl_add_u64 v[10:11], v[4:5], 0, v[10:11]
	v_lshl_add_u64 v[12:13], v[4:5], 0, v[12:13]
	v_lshl_add_u64 v[14:15], v[4:5], 0, v[14:15]
	v_lshl_add_u64 v[16:17], v[4:5], 0, v[16:17]
	v_lshl_add_u64 v[18:19], v[4:5], 0, v[18:19]
	v_lshl_add_u64 v[20:21], v[4:5], 0, v[20:21]
	v_lshl_add_u64 v[4:5], v[4:5], 0, v[6:7]
	global_load_dword v6, v[8:9], off nt
	global_load_dword v7, v[10:11], off nt
	global_load_dword v22, v[12:13], off nt
	global_load_dword v23, v[14:15], off nt
	global_load_dword v32, v[16:17], off nt
	global_load_dword v33, v[18:19], off nt
	global_load_dword v34, v[20:21], off nt
	global_load_dword v35, v[4:5], off nt
	s_movk_i32 s1, 0x104
	v_mad_u32_u24 v1, v1, s1, v2
	s_ashr_i32 s3, s2, 31
	s_lshl_b64 s[2:3], s[2:3], 1
	s_add_u32 s2, s6, s2
	s_addc_u32 s3, s7, s3
	s_waitcnt vmcnt(15)
	ds_write_b32 v1, v24
	s_waitcnt vmcnt(14)
	ds_write_b32 v1, v25 offset:1040
	s_waitcnt vmcnt(13)
	ds_write_b32 v1, v26 offset:2080
	s_waitcnt vmcnt(12)
	ds_write_b32 v1, v27 offset:3120
	s_waitcnt vmcnt(11)
	ds_write_b32 v1, v28 offset:4160
	s_waitcnt vmcnt(10)
	ds_write_b32 v1, v29 offset:5200
	s_waitcnt vmcnt(9)
	ds_write_b32 v1, v30 offset:6240
	s_waitcnt vmcnt(8)
	ds_write_b32 v1, v31 offset:7280
	s_waitcnt vmcnt(7)
	ds_write_b32 v1, v6 offset:8320
	s_waitcnt vmcnt(6)
	ds_write_b32 v1, v7 offset:9360
	s_waitcnt vmcnt(5)
	ds_write_b32 v1, v22 offset:10400
	s_waitcnt vmcnt(4)
	ds_write_b32 v1, v23 offset:11440
	s_waitcnt vmcnt(3)
	ds_write_b32 v1, v32 offset:12480
	s_waitcnt vmcnt(2)
	ds_write_b32 v1, v33 offset:13520
	s_waitcnt vmcnt(1)
	ds_write_b32 v1, v34 offset:14560
	s_waitcnt vmcnt(0)
	ds_write_b32 v1, v35 offset:15600
	v_lshrrev_b32_e32 v22, 3, v0
	v_lshlrev_b32_e32 v0, 3, v0
	v_and_b32_e32 v0, 56, v0
	v_lshlrev_b32_e32 v2, 1, v0
	v_mul_u32_u24_e32 v0, 0x104, v0
	v_lshl_add_u32 v0, v22, 2, v0
	v_add_u32_e32 v1, 0x400, v0
	s_waitcnt lgkmcnt(0)
	s_barrier
	ds_read2_b32 v[4:5], v0 offset1:32
	ds_read2_b32 v[6:7], v0 offset0:130 offset1:162
	ds_read2_b32 v[8:9], v1 offset0:4 offset1:36
	ds_read2_b32 v[10:11], v1 offset0:134 offset1:166
	ds_read2_b32 v[12:13], v1 offset0:199 offset1:231
	ds_read2_b32 v[14:15], v1 offset0:69 offset1:101
	ds_read2_b32 v[16:17], v0 offset0:195 offset1:227
	ds_read2_b32 v[18:19], v0 offset0:65 offset1:97
	v_lshl_add_u64 v[20:21], s[2:3], 0, v[2:3]
	s_waitcnt lgkmcnt(3)
	v_cvt_pk_f16_f32 v3, v10, v12
	s_waitcnt lgkmcnt(2)
	v_cvt_pk_f16_f32 v2, v8, v14
	s_waitcnt lgkmcnt(1)
	v_cvt_pk_f16_f32 v1, v6, v16
	s_waitcnt lgkmcnt(0)
	v_cvt_pk_f16_f32 v0, v4, v18
	v_or_b32_e32 v4, s0, v22
	s_movk_i32 s0, 0x600
	v_mul_lo_u32 v22, v4, s0
	v_ashrrev_i32_e32 v23, 31, v22
	v_lshl_add_u64 v[24:25], v[22:23], 1, v[20:21]
	v_add_u32_e32 v4, 0xc000, v22
	global_store_dwordx4 v[24:25], v[0:3], off
	s_nop 1
	v_cvt_pk_f16_f32 v0, v5, v19
	v_ashrrev_i32_e32 v5, 31, v4
	v_cvt_pk_f16_f32 v3, v11, v13
	v_cvt_pk_f16_f32 v2, v9, v15
	v_cvt_pk_f16_f32 v1, v7, v17
	v_lshl_add_u64 v[4:5], v[4:5], 1, v[20:21]
	global_store_dwordx4 v[4:5], v[0:3], off
	s_endpgm
